# E6 with the whole kernel shifted by 16 bytes (4 s_nop at entry): code-placement sweep
# speedup vs baseline: 1.0119x; 1.0014x over previous
_Z3fwd4Args:
	s_nop 0
	s_nop 0
	s_nop 0
	s_nop 0
	v_lshl_add_u32 v1, v0, 2, 0
	v_add_u32_e32 v1, 0x20000, v1
	v_mov_b32_e32 v2, 0
	s_mov_b32 s10, s2
	ds_write2st64_b32 v1, v2, v2 offset1:8
	ds_write2st64_b32 v1, v2, v2 offset0:16 offset1:24
	v_or_b32_e32 v1, 0x800, v0
	s_mov_b64 s[2:3], -1
	s_and_saveexec_b64 s[4:5], s[2:3]
	v_lshl_add_u32 v3, v1, 2, 0
	v_add_u32_e32 v3, 0x20000, v3
	ds_write_b32 v3, v2
	s_or_b64 exec, exec, s[4:5]
	s_and_saveexec_b64 s[4:5], s[2:3]
	s_add_i32 s2, 0, 0x20000
	v_lshl_add_u32 v1, v1, 2, s2
	v_mov_b32_e32 v2, 0
	ds_write_b32 v1, v2 offset:2048
	s_or_b64 exec, exec, s[4:5]
	v_or_b32_e32 v1, 0xc00, v0
	v_cmp_gt_u32_e64 s[2:3], 7, 6
	v_cmp_gt_u32_e64 s[6:7], 7, 5
	s_and_saveexec_b64 s[4:5], s[6:7]
	v_lshl_add_u32 v2, v1, 2, 0
	v_add_u32_e32 v2, 0x20000, v2
	v_mov_b32_e32 v3, 0
	ds_write_b32 v2, v3
	s_or_b64 exec, exec, s[4:5]
	s_and_saveexec_b64 s[4:5], s[2:3]
	s_add_i32 s2, 0, 0x20000
	v_lshl_add_u32 v1, v1, 2, s2
	v_mov_b32_e32 v2, 0
	ds_write_b32 v1, v2 offset:2048
	s_or_b64 exec, exec, s[4:5]
	v_cmp_eq_u32_e32 vcc, 0, v0
	s_waitcnt lgkmcnt(0)
	s_barrier
	s_and_saveexec_b64 s[2:3], vcc
	s_cbranch_execz .LBB0_10
	s_load_dwordx16 s[12:27], s[0:1], 0x0
	s_add_i32 s4, 0, 0x201c0
	s_load_dwordx16 s[36:51], s[0:1], 0x40
	v_mov_b32_e32 v1, s4
	s_add_i32 s4, 0, 0x201d0
	s_waitcnt lgkmcnt(0)
	v_mov_b32_e32 v2, s12
	v_mov_b32_e32 v3, s13
	v_mov_b32_e32 v4, s14
	v_mov_b32_e32 v5, s15
	ds_write_b128 v1, v[2:5]
	v_mov_b32_e32 v2, s16
	v_mov_b32_e32 v3, s17
	v_mov_b32_e32 v4, s18
	v_mov_b32_e32 v5, s19
	v_mov_b32_e32 v1, s4
	s_add_i32 s4, 0, 0x201e0
	ds_write_b128 v1, v[2:5]
	v_mov_b32_e32 v2, s20
	v_mov_b32_e32 v3, s21
	v_mov_b32_e32 v4, s22
	v_mov_b32_e32 v5, s23
	v_mov_b32_e32 v1, s4
	s_add_i32 s4, 0, 0x201f0
	ds_write_b128 v1, v[2:5]
	v_mov_b32_e32 v2, s24
	v_mov_b32_e32 v3, s25
	v_mov_b32_e32 v4, s26
	v_mov_b32_e32 v5, s27
	v_mov_b32_e32 v1, s4
	s_add_i32 s4, 0, 0x20200
	s_load_dwordx16 s[12:27], s[0:1], 0x80
	ds_write_b128 v1, v[2:5]
	v_mov_b32_e32 v2, s36
	v_mov_b32_e32 v3, s37
	v_mov_b32_e32 v4, s38
	v_mov_b32_e32 v5, s39
	v_mov_b32_e32 v1, s4
	s_add_i32 s4, 0, 0x20210
	ds_write_b128 v1, v[2:5]
	v_mov_b32_e32 v2, s40
	v_mov_b32_e32 v3, s41
	v_mov_b32_e32 v4, s42
	v_mov_b32_e32 v5, s43
	v_mov_b32_e32 v1, s4
	s_add_i32 s4, 0, 0x20220
	ds_write_b128 v1, v[2:5]
	v_mov_b32_e32 v2, s44
	v_mov_b32_e32 v3, s45
	v_mov_b32_e32 v4, s46
	v_mov_b32_e32 v5, s47
	v_mov_b32_e32 v1, s4
	s_add_i32 s4, 0, 0x20230
	ds_write_b128 v1, v[2:5]
	v_mov_b32_e32 v2, s48
	v_mov_b32_e32 v3, s49
	v_mov_b32_e32 v4, s50
	v_mov_b32_e32 v5, s51
	v_mov_b32_e32 v1, s4
	s_add_i32 s4, 0, 0x20240
	ds_write_b128 v1, v[2:5]
	s_waitcnt lgkmcnt(0)
	v_mov_b32_e32 v2, s12
	v_mov_b32_e32 v3, s13
	v_mov_b32_e32 v4, s14
	v_mov_b32_e32 v5, s15
	v_mov_b32_e32 v1, s4
	s_add_i32 s4, 0, 0x20250
	ds_write_b128 v1, v[2:5]
	v_mov_b32_e32 v2, s16
	v_mov_b32_e32 v3, s17
	v_mov_b32_e32 v4, s18
	v_mov_b32_e32 v5, s19
	v_mov_b32_e32 v1, s4
	s_add_i32 s4, 0, 0x20260
	ds_write_b128 v1, v[2:5]
	v_mov_b32_e32 v1, s4
	s_load_dwordx2 s[4:5], s[0:1], 0xc0
	v_mov_b32_e32 v2, s20
	v_mov_b32_e32 v3, s21
	v_mov_b32_e32 v4, s22
	v_mov_b32_e32 v5, s23
	s_add_i32 s6, 0, 0x20270
	ds_write_b128 v1, v[2:5]
	v_mov_b32_e32 v2, s24
	v_mov_b32_e32 v3, s25
	v_mov_b32_e32 v4, s26
	v_mov_b32_e32 v5, s27
	v_mov_b32_e32 v1, s6
	s_add_i32 s6, 0, 0x20280
	ds_write_b128 v1, v[2:5]
	v_mov_b32_e32 v1, s6
	s_waitcnt lgkmcnt(0)
	v_mov_b64_e32 v[2:3], s[4:5]
	ds_write_b64 v1, v[2:3]
